# first own k-step carries 3 relu/cvt VALU per MFMA so the second tile pair is stored to LDS earlier
# speedup vs baseline: 1.0028x; 1.0028x over previous
.LBB1_4:
	s_and_saveexec_b64 s[32:33], s[2:3]
	v_perm_b32 v5, v1, v102, s23
	v_perm_b32 v9, v121, v103, s23
	s_or_b64 exec, exec, s[32:33]
	v_mov_b32_e32 v144, v1
	v_mov_b32_e32 v145, v121
	v_mfma_f32_16x16x32_f16 v[164:167], v[30:33], v[2:5], 0
	v_mfma_f32_16x16x32_f16 v[180:183], v[22:25], v[2:5], 0
	s_cmp_lg_u32 s22, 0x818000
	v_permlane32_swap_b32_e32 v1, v144
	v_permlane32_swap_b32_e32 v121, v145
	v_mfma_f32_16x16x32_f16 v[168:171], v[30:33], v[6:9], 0
	v_mfma_f32_16x16x32_f16 v[184:187], v[22:25], v[6:9], 0
	s_cselect_b32 s9, s11, 15
	s_and_saveexec_b64 s[32:33], s[2:3]
	v_perm_b32 v17, v144, v115, s23
	v_perm_b32 v29, v145, v116, s23
	s_or_b64 exec, exec, s[32:33]
	v_mfma_f32_16x16x32_f16 v[172:175], v[30:33], v[14:17], 0
	v_mfma_f32_16x16x32_f16 v[188:191], v[22:25], v[14:17], 0
	v_mfma_f32_16x16x32_f16 v[176:179], v[30:33], v[26:29], 0
	v_mfma_f32_16x16x32_f16 v[192:195], v[22:25], v[26:29], 0
	v_mfma_f32_16x16x32_f16 v[208:211], v[18:21], v[2:5], 0
	v_mfma_f32_16x16x32_f16 v[224:227], v[10:13], v[2:5], 0
	v_cvt_pk_f16_f32 v122, v164, v165
	v_cvt_pk_f16_f32 v123, v166, v167
	v_pk_max_f16 v122, v122, 0
	v_pk_max_f16 v123, v123, 0
	v_cvt_pk_f16_f32 v124, v180, v181
	v_cvt_pk_f16_f32 v125, v182, v183
	v_pk_max_f16 v124, v124, 0
	v_pk_max_f16 v125, v125, 0
	ds_write_b128 v107, v[122:125]
	v_mfma_f32_16x16x32_f16 v[212:215], v[18:21], v[6:9], 0
	v_mfma_f32_16x16x32_f16 v[228:231], v[10:13], v[6:9], 0
	v_cvt_pk_f16_f32 v126, v168, v169
	v_cvt_pk_f16_f32 v127, v170, v171
	v_pk_max_f16 v126, v126, 0
	v_pk_max_f16 v127, v127, 0
	v_cvt_pk_f16_f32 v128, v184, v185
	v_cvt_pk_f16_f32 v129, v186, v187
	v_pk_max_f16 v128, v128, 0
	v_pk_max_f16 v129, v129, 0
	ds_write_b128 v107, v[126:129] offset:16384
	v_mfma_f32_16x16x32_f16 v[216:219], v[18:21], v[14:17], 0
	v_mfma_f32_16x16x32_f16 v[232:235], v[10:13], v[14:17], 0
	v_cvt_pk_f16_f32 v134, v172, v173
	v_cvt_pk_f16_f32 v135, v174, v175
	v_pk_max_f16 v134, v134, 0
	v_pk_max_f16 v135, v135, 0
	v_cvt_pk_f16_f32 v136, v188, v189
	v_cvt_pk_f16_f32 v137, v190, v191
	v_pk_max_f16 v136, v136, 0
	v_pk_max_f16 v137, v137, 0
	ds_write_b128 v107, v[134:137] offset:32768
	v_mfma_f32_16x16x32_f16 v[220:223], v[18:21], v[26:29], 0
	v_mfma_f32_16x16x32_f16 v[236:239], v[10:13], v[26:29], 0
	v_cvt_pk_f16_f32 v138, v176, v177
	v_cvt_pk_f16_f32 v139, v178, v179
	v_pk_max_f16 v138, v138, 0
	v_pk_max_f16 v139, v139, 0
	v_cvt_pk_f16_f32 v140, v192, v193
	v_cvt_pk_f16_f32 v141, v194, v195
	v_pk_max_f16 v140, v140, 0
	v_pk_max_f16 v141, v141, 0
	ds_write_b128 v107, v[138:141] offset:49152
	v_add_u32_e32 v111, s64, v111
	v_add_u32_e32 v98, s65, v98
	s_lshl_b32 s20, s9, 7
	v_lshl_add_u64 v[0:1], s[20:21], 3, v[132:133]
	s_add_i32 s25, s22, s34
	s_lshl_b32 s8, s9, 8
	buffer_load_dwordx4 v[192:195], v147, s[16:19], s25 offen
	buffer_load_dwordx4 v[196:199], v148, s[16:19], s25 offen
	buffer_load_dwordx4 v[200:203], v149, s[16:19], s25 offen
	buffer_load_dwordx4 v[204:207], v150, s[16:19], s25 offen
	s_waitcnt vmcnt(19)
	v_mfma_f32_16x16x32_f16 v[164:167], v[58:61], v[122:125], v[240:243]
	v_cvt_pk_f16_f32 v142, v208, v209
	v_cvt_pk_f16_f32 v143, v210, v211
	v_pk_max_f16 v142, v142, 0
	v_mfma_f32_16x16x32_f16 v[168:171], v[58:61], v[126:129], v[240:243]
	v_pk_max_f16 v143, v143, 0
	v_cvt_pk_f16_f32 v144, v224, v225
	v_cvt_pk_f16_f32 v145, v226, v227
	v_mfma_f32_16x16x32_f16 v[172:175], v[58:61], v[134:137], v[240:243]
	v_pk_max_f16 v144, v144, 0
	v_pk_max_f16 v145, v145, 0
	v_cvt_pk_f16_f32 v152, v212, v213
	ds_write_b128 v108, v[142:145]
	v_mfma_f32_16x16x32_f16 v[10:13], v[58:61], v[138:141], v[240:243]
	v_cvt_pk_f16_f32 v153, v214, v215
	v_pk_max_f16 v152, v152, 0
	v_pk_max_f16 v153, v153, 0
	s_waitcnt vmcnt(18)
	v_mfma_f32_16x16x32_f16 v[58:61], v[54:57], v[122:125], v[244:247]
	v_cvt_pk_f16_f32 v154, v228, v229
	v_cvt_pk_f16_f32 v155, v230, v231
	v_pk_max_f16 v154, v154, 0
	v_mfma_f32_16x16x32_f16 v[176:179], v[54:57], v[126:129], v[244:247]
	v_pk_max_f16 v155, v155, 0
	v_cvt_pk_f16_f32 v156, v216, v217
	v_cvt_pk_f16_f32 v157, v218, v219
	ds_write_b128 v108, v[152:155] offset:16384
	v_mfma_f32_16x16x32_f16 v[180:183], v[54:57], v[134:137], v[244:247]
	v_pk_max_f16 v156, v156, 0
	v_pk_max_f16 v157, v157, 0
	v_cvt_pk_f16_f32 v158, v232, v233
	v_mfma_f32_16x16x32_f16 v[18:21], v[54:57], v[138:141], v[244:247]
	v_cvt_pk_f16_f32 v159, v234, v235
	v_pk_max_f16 v158, v158, 0
	v_pk_max_f16 v159, v159, 0
	ds_write_b128 v108, v[156:159] offset:32768
	s_waitcnt vmcnt(17)
	v_mfma_f32_16x16x32_f16 v[54:57], v[50:53], v[122:125], v[248:251]
	v_cvt_pk_f16_f32 v160, v220, v221
	v_cvt_pk_f16_f32 v161, v222, v223
	v_pk_max_f16 v160, v160, 0
	v_mfma_f32_16x16x32_f16 v[184:187], v[50:53], v[126:129], v[248:251]
	v_pk_max_f16 v161, v161, 0
	v_cvt_pk_f16_f32 v162, v236, v237
	v_cvt_pk_f16_f32 v163, v238, v239
	v_mfma_f32_16x16x32_f16 v[188:191], v[50:53], v[134:137], v[248:251]
	v_pk_max_f16 v162, v162, 0
	v_pk_max_f16 v163, v163, 0
	ds_write_b128 v108, v[160:163] offset:49152
	v_mfma_f32_16x16x32_f16 v[22:25], v[50:53], v[138:141], v[248:251]

	s_waitcnt vmcnt(16)
	v_mfma_f32_16x16x32_f16 v[50:53], v[38:41], v[122:125], v[252:255]

	v_mfma_f32_16x16x32_f16 v[122:125], v[38:41], v[126:129], v[252:255]

	v_mfma_f32_16x16x32_f16 v[126:129], v[38:41], v[134:137], v[252:255]

	v_mfma_f32_16x16x32_f16 v[38:41], v[38:41], v[138:141], v[252:255]

	s_add_i32 s9, s22, s35
	s_waitcnt vmcnt(15)
	v_mfma_f32_16x16x32_f16 v[164:167], v[94:97], v[142:145], v[164:167]
	v_mfma_f32_16x16x32_f16 v[168:171], v[94:97], v[152:155], v[168:171]
	s_waitcnt vmcnt(14)
	v_mfma_f32_16x16x32_f16 v[58:61], v[90:93], v[142:145], v[58:61]
	v_mfma_f32_16x16x32_f16 v[176:179], v[90:93], v[152:155], v[176:179]
	s_waitcnt vmcnt(13)
	v_mfma_f32_16x16x32_f16 v[54:57], v[78:81], v[142:145], v[54:57]
	v_mfma_f32_16x16x32_f16 v[184:187], v[78:81], v[152:155], v[184:187]
	s_waitcnt vmcnt(12)
	v_mfma_f32_16x16x32_f16 v[50:53], v[34:37], v[142:145], v[50:53]
	buffer_load_dwordx4 v[140:143], v147, s[16:19], s9 offen
	buffer_load_dwordx4 v[220:223], v148, s[16:19], s9 offen
	v_mfma_f32_16x16x32_f16 v[122:125], v[34:37], v[152:155], v[122:125]
	buffer_load_dwordx4 v[152:155], v149, s[16:19], s9 offen
	buffer_load_dwordx4 v[224:227], v150, s[16:19], s9 offen
	s_mov_b32 s9, s21
	s_waitcnt lgkmcnt(0)
	s_barrier
	v_add_u32_e32 v99, s66, v99
	ds_read_b128 v[136:139], v99
	ds_read_b128 v[208:211], v99 offset:16384
	ds_read_b128 v[212:215], v99 offset:32768
	ds_read_b128 v[216:219], v99 offset:49152
	v_mfma_f32_16x16x32_f16 v[172:175], v[94:97], v[156:159], v[172:175]
	v_mfma_f32_16x16x32_f16 v[94:97], v[94:97], v[160:163], v[10:13]
	s_nop 2
	v_lshl_add_u64 v[10:11], s[8:9], 4, v[130:131]
	v_mfma_f32_16x16x32_f16 v[180:183], v[90:93], v[156:159], v[180:183]
	v_mfma_f32_16x16x32_f16 v[90:93], v[90:93], v[160:163], v[18:21]
	v_mfma_f32_16x16x32_f16 v[188:191], v[78:81], v[156:159], v[188:191]
	v_mfma_f32_16x16x32_f16 v[78:81], v[78:81], v[160:163], v[22:25]
	global_load_dwordx4 v[30:33], v[10:11], off
	s_nop 1
	global_load_dwordx4 v[22:25], v[10:11], off offset:1024
	global_load_dwordx4 v[18:21], v[10:11], off offset:2048
	s_nop 0
	global_load_dwordx4 v[10:13], v[10:11], off offset:3072
	s_nop 0
	global_load_dwordx2 v[134:135], v[0:1], off
	v_mfma_f32_16x16x32_f16 v[126:129], v[34:37], v[156:159], v[126:129]
	v_mfma_f32_16x16x32_f16 v[34:37], v[34:37], v[160:163], v[38:41]
	s_nop 2
	v_add_u32_e32 v100, s67, v100
	ds_read_b128 v[38:41], v100
	ds_read_b128 v[156:159], v100 offset:16384
	ds_read_b128 v[160:163], v100 offset:32768
	ds_read_b128 v[228:231], v100 offset:49152
	s_add_i32 s8, s22, s36
	s_waitcnt vmcnt(20) lgkmcnt(7)
	v_mfma_f32_16x16x32_f16 v[164:167], v[82:85], v[136:139], v[164:167]
	s_waitcnt lgkmcnt(6)
	v_mfma_f32_16x16x32_f16 v[168:171], v[82:85], v[208:211], v[168:171]
	s_waitcnt lgkmcnt(5)
	v_mfma_f32_16x16x32_f16 v[172:175], v[82:85], v[212:215], v[172:175]
	s_waitcnt lgkmcnt(4)
	v_mfma_f32_16x16x32_f16 v[82:85], v[82:85], v[216:219], v[94:97]
	s_waitcnt vmcnt(19)
	v_mfma_f32_16x16x32_f16 v[58:61], v[70:73], v[136:139], v[58:61]
	v_mfma_f32_16x16x32_f16 v[94:97], v[70:73], v[208:211], v[176:179]
	v_mfma_f32_16x16x32_f16 v[176:179], v[70:73], v[212:215], v[180:183]
	v_mfma_f32_16x16x32_f16 v[70:73], v[70:73], v[216:219], v[90:93]
	s_waitcnt vmcnt(18)
	v_mfma_f32_16x16x32_f16 v[54:57], v[62:65], v[136:139], v[54:57]
	v_mfma_f32_16x16x32_f16 v[90:93], v[62:65], v[208:211], v[184:187]
	v_mfma_f32_16x16x32_f16 v[180:183], v[62:65], v[212:215], v[188:191]
	v_mfma_f32_16x16x32_f16 v[62:65], v[62:65], v[216:219], v[78:81]
	s_waitcnt vmcnt(17)
	v_mfma_f32_16x16x32_f16 v[50:53], v[42:45], v[136:139], v[50:53]
	v_mfma_f32_16x16x32_f16 v[78:81], v[42:45], v[208:211], v[122:125]
	v_mfma_f32_16x16x32_f16 v[122:125], v[42:45], v[212:215], v[126:129]
	s_nop 2
	buffer_load_dwordx4 v[126:129], v147, s[16:19], s8 offen
	buffer_load_dwordx4 v[136:139], v148, s[16:19], s8 offen
	buffer_load_dwordx4 v[184:187], v149, s[16:19], s8 offen
	buffer_load_dwordx4 v[188:191], v150, s[16:19], s8 offen
	v_mfma_f32_16x16x32_f16 v[34:37], v[42:45], v[216:219], v[34:37]
	v_add_u32_e32 v111, s68, v111
	ds_read_b128 v[42:45], v111
	ds_read_b128 v[208:211], v111 offset:16384
	ds_read_b128 v[212:215], v111 offset:32768
	ds_read_b128 v[216:219], v111 offset:49152
	s_add_i32 s8, s22, s37
	s_waitcnt vmcnt(20) lgkmcnt(7)
	v_mfma_f32_16x16x32_f16 v[164:167], v[86:89], v[38:41], v[164:167]
	s_waitcnt lgkmcnt(6)
	v_mfma_f32_16x16x32_f16 v[168:171], v[86:89], v[156:159], v[168:171]
	s_waitcnt lgkmcnt(5)
	v_mfma_f32_16x16x32_f16 v[172:175], v[86:89], v[160:163], v[172:175]
	s_waitcnt lgkmcnt(4)
	v_mfma_f32_16x16x32_f16 v[82:85], v[86:89], v[228:231], v[82:85]
	s_waitcnt vmcnt(19)
	v_mfma_f32_16x16x32_f16 v[58:61], v[74:77], v[38:41], v[58:61]
	v_mfma_f32_16x16x32_f16 v[86:89], v[74:77], v[156:159], v[94:97]
	v_mfma_f32_16x16x32_f16 v[94:97], v[74:77], v[160:163], v[176:179]
	v_mfma_f32_16x16x32_f16 v[70:73], v[74:77], v[228:231], v[70:73]
	s_waitcnt vmcnt(18)
	v_mfma_f32_16x16x32_f16 v[54:57], v[66:69], v[38:41], v[54:57]
	v_mfma_f32_16x16x32_f16 v[74:77], v[66:69], v[156:159], v[90:93]
	v_mfma_f32_16x16x32_f16 v[90:93], v[66:69], v[160:163], v[180:183]
	v_mfma_f32_16x16x32_f16 v[62:65], v[66:69], v[228:231], v[62:65]
	s_waitcnt vmcnt(17)
	v_mfma_f32_16x16x32_f16 v[38:41], v[46:49], v[38:41], v[50:53]
	v_mfma_f32_16x16x32_f16 v[50:53], v[46:49], v[156:159], v[78:81]
	v_mfma_f32_16x16x32_f16 v[66:69], v[46:49], v[160:163], v[122:125]
	s_nop 1
	buffer_load_dwordx4 v[78:81], v147, s[16:19], s8 offen
	buffer_load_dwordx4 v[122:125], v148, s[16:19], s8 offen
	buffer_load_dwordx4 v[156:159], v149, s[16:19], s8 offen
	buffer_load_dwordx4 v[160:163], v150, s[16:19], s8 offen
	v_mfma_f32_16x16x32_f16 v[34:37], v[46:49], v[228:231], v[34:37]
	v_add_u32_e32 v98, s69, v98
	ds_read_b128 v[46:49], v98
	ds_read_b128 v[176:179], v98 offset:16384
	ds_read_b128 v[180:183], v98 offset:32768
	ds_read_b128 v[228:231], v98 offset:49152
	s_add_i32 s8, s22, s38
	s_waitcnt vmcnt(20) lgkmcnt(7)
	v_mfma_f32_16x16x32_f16 v[164:167], v[192:195], v[42:45], v[164:167]
	s_waitcnt lgkmcnt(6)
	v_mfma_f32_16x16x32_f16 v[168:171], v[192:195], v[208:211], v[168:171]
	s_waitcnt lgkmcnt(5)
	v_mfma_f32_16x16x32_f16 v[172:175], v[192:195], v[212:215], v[172:175]
	s_waitcnt lgkmcnt(4)
	v_mfma_f32_16x16x32_f16 v[82:85], v[192:195], v[216:219], v[82:85]
	s_waitcnt vmcnt(19)
	v_mfma_f32_16x16x32_f16 v[58:61], v[196:199], v[42:45], v[58:61]
	v_mfma_f32_16x16x32_f16 v[86:89], v[196:199], v[208:211], v[86:89]
	v_mfma_f32_16x16x32_f16 v[94:97], v[196:199], v[212:215], v[94:97]
	v_mfma_f32_16x16x32_f16 v[70:73], v[196:199], v[216:219], v[70:73]
	s_waitcnt vmcnt(18)
	v_mfma_f32_16x16x32_f16 v[54:57], v[200:203], v[42:45], v[54:57]
	v_mfma_f32_16x16x32_f16 v[74:77], v[200:203], v[208:211], v[74:77]
	v_mfma_f32_16x16x32_f16 v[90:93], v[200:203], v[212:215], v[90:93]
	v_mfma_f32_16x16x32_f16 v[62:65], v[200:203], v[216:219], v[62:65]
	s_waitcnt vmcnt(17)
	v_mfma_f32_16x16x32_f16 v[38:41], v[204:207], v[42:45], v[38:41]
	v_mfma_f32_16x16x32_f16 v[42:45], v[204:207], v[208:211], v[50:53]
	v_mfma_f32_16x16x32_f16 v[50:53], v[204:207], v[212:215], v[66:69]
	s_nop 2
	buffer_load_dwordx4 v[66:69], v147, s[16:19], s8 offen
	buffer_load_dwordx4 v[192:195], v148, s[16:19], s8 offen
	buffer_load_dwordx4 v[196:199], v149, s[16:19], s8 offen
	buffer_load_dwordx4 v[200:203], v150, s[16:19], s8 offen
	v_mfma_f32_16x16x32_f16 v[34:37], v[204:207], v[216:219], v[34:37]
	v_add_u32_e32 v99, s70, v99
	ds_read_b128 v[204:207], v99
	ds_read_b128 v[208:211], v99 offset:16384
	ds_read_b128 v[212:215], v99 offset:32768
	ds_read_b128 v[216:219], v99 offset:49152
	s_add_i32 s8, s22, s39
	s_waitcnt vmcnt(20) lgkmcnt(7)
	v_mfma_f32_16x16x32_f16 v[164:167], v[140:143], v[46:49], v[164:167]
	s_waitcnt lgkmcnt(6)
	v_mfma_f32_16x16x32_f16 v[168:171], v[140:143], v[176:179], v[168:171]
	s_waitcnt lgkmcnt(5)
	v_mfma_f32_16x16x32_f16 v[172:175], v[140:143], v[180:183], v[172:175]
	s_waitcnt lgkmcnt(4)
	v_mfma_f32_16x16x32_f16 v[82:85], v[140:143], v[228:231], v[82:85]
	s_waitcnt vmcnt(19)
	v_mfma_f32_16x16x32_f16 v[58:61], v[220:223], v[46:49], v[58:61]
	v_mfma_f32_16x16x32_f16 v[86:89], v[220:223], v[176:179], v[86:89]
	s_waitcnt vmcnt(18)
	v_mfma_f32_16x16x32_f16 v[54:57], v[152:155], v[46:49], v[54:57]
	v_mfma_f32_16x16x32_f16 v[74:77], v[152:155], v[176:179], v[74:77]
	v_mfma_f32_16x16x32_f16 v[90:93], v[152:155], v[180:183], v[90:93]
	v_mfma_f32_16x16x32_f16 v[62:65], v[152:155], v[228:231], v[62:65]
	s_waitcnt vmcnt(17)
	v_mfma_f32_16x16x32_f16 v[38:41], v[224:227], v[46:49], v[38:41]
	v_mfma_f32_16x16x32_f16 v[42:45], v[224:227], v[176:179], v[42:45]
	v_mfma_f32_16x16x32_f16 v[46:49], v[224:227], v[180:183], v[50:53]
	s_nop 2
	buffer_load_dwordx4 v[50:53], v147, s[16:19], s8 offen
	buffer_load_dwordx4 v[140:143], v148, s[16:19], s8 offen
	buffer_load_dwordx4 v[152:155], v149, s[16:19], s8 offen
	buffer_load_dwordx4 v[176:179], v150, s[16:19], s8 offen
	v_mfma_f32_16x16x32_f16 v[94:97], v[220:223], v[180:183], v[94:97]
	v_mfma_f32_16x16x32_f16 v[70:73], v[220:223], v[228:231], v[70:73]
	v_mfma_f32_16x16x32_f16 v[34:37], v[224:227], v[228:231], v[34:37]
	v_add_u32_e32 v100, s71, v100
	ds_read_b128 v[180:183], v100
	ds_read_b128 v[220:223], v100 offset:16384
	ds_read_b128 v[224:227], v100 offset:32768
	ds_read_b128 v[228:231], v100 offset:49152
	s_add_i32 s8, s22, s40
	s_waitcnt vmcnt(15) lgkmcnt(7)
	v_mfma_f32_16x16x32_f16 v[164:167], v[126:129], v[204:207], v[164:167]
	s_waitcnt lgkmcnt(6)
	v_mfma_f32_16x16x32_f16 v[168:171], v[126:129], v[208:211], v[168:171]
	s_waitcnt lgkmcnt(5)
	v_mfma_f32_16x16x32_f16 v[172:175], v[126:129], v[212:215], v[172:175]
	s_waitcnt lgkmcnt(4)
	v_mfma_f32_16x16x32_f16 v[82:85], v[126:129], v[216:219], v[82:85]
	s_waitcnt vmcnt(14)
	v_mfma_f32_16x16x32_f16 v[58:61], v[136:139], v[204:207], v[58:61]
	v_mfma_f32_16x16x32_f16 v[86:89], v[136:139], v[208:211], v[86:89]
	v_mfma_f32_16x16x32_f16 v[94:97], v[136:139], v[212:215], v[94:97]
	v_mfma_f32_16x16x32_f16 v[70:73], v[136:139], v[216:219], v[70:73]
	s_waitcnt vmcnt(13)
	v_mfma_f32_16x16x32_f16 v[54:57], v[184:187], v[204:207], v[54:57]
	v_mfma_f32_16x16x32_f16 v[74:77], v[184:187], v[208:211], v[74:77]
	v_mfma_f32_16x16x32_f16 v[90:93], v[184:187], v[212:215], v[90:93]
	v_mfma_f32_16x16x32_f16 v[62:65], v[184:187], v[216:219], v[62:65]
	s_waitcnt vmcnt(12)
	v_mfma_f32_16x16x32_f16 v[38:41], v[188:191], v[204:207], v[38:41]
	buffer_load_dwordx4 v[126:129], v147, s[16:19], s8 offen
	buffer_load_dwordx4 v[136:139], v148, s[16:19], s8 offen
	buffer_load_dwordx4 v[184:187], v149, s[16:19], s8 offen
	buffer_load_dwordx4 v[204:207], v150, s[16:19], s8 offen
	v_mfma_f32_16x16x32_f16 v[42:45], v[188:191], v[208:211], v[42:45]
	v_mfma_f32_16x16x32_f16 v[46:49], v[188:191], v[212:215], v[46:49]
	v_mfma_f32_16x16x32_f16 v[34:37], v[188:191], v[216:219], v[34:37]
	v_add_u32_e32 v111, s72, v111
	ds_read_b128 v[188:191], v111
	ds_read_b128 v[208:211], v111 offset:16384
	ds_read_b128 v[212:215], v111 offset:32768
	ds_read_b128 v[216:219], v111 offset:49152
	s_add_i32 s8, s22, s41
	s_waitcnt vmcnt(15) lgkmcnt(7)
	v_mfma_f32_16x16x32_f16 v[164:167], v[78:81], v[180:183], v[164:167]
	s_waitcnt lgkmcnt(6)
	v_mfma_f32_16x16x32_f16 v[168:171], v[78:81], v[220:223], v[168:171]
	s_waitcnt lgkmcnt(5)
	v_mfma_f32_16x16x32_f16 v[172:175], v[78:81], v[224:227], v[172:175]
	s_waitcnt lgkmcnt(4)
	v_mfma_f32_16x16x32_f16 v[78:81], v[78:81], v[228:231], v[82:85]
	s_waitcnt vmcnt(14)
	v_mfma_f32_16x16x32_f16 v[58:61], v[122:125], v[180:183], v[58:61]
	v_mfma_f32_16x16x32_f16 v[82:85], v[122:125], v[220:223], v[86:89]
	v_mfma_f32_16x16x32_f16 v[86:89], v[122:125], v[224:227], v[94:97]
	v_mfma_f32_16x16x32_f16 v[70:73], v[122:125], v[228:231], v[70:73]
	s_waitcnt vmcnt(13)
	v_mfma_f32_16x16x32_f16 v[54:57], v[156:159], v[180:183], v[54:57]
	v_mfma_f32_16x16x32_f16 v[74:77], v[156:159], v[220:223], v[74:77]
	v_mfma_f32_16x16x32_f16 v[90:93], v[156:159], v[224:227], v[90:93]
	v_mfma_f32_16x16x32_f16 v[62:65], v[156:159], v[228:231], v[62:65]
	s_waitcnt vmcnt(12)
	v_mfma_f32_16x16x32_f16 v[38:41], v[160:163], v[180:183], v[38:41]
	buffer_load_dwordx4 v[94:97], v147, s[16:19], s8 offen
	buffer_load_dwordx4 v[122:125], v148, s[16:19], s8 offen
	buffer_load_dwordx4 v[156:159], v149, s[16:19], s8 offen
	buffer_load_dwordx4 v[180:183], v150, s[16:19], s8 offen
	v_mfma_f32_16x16x32_f16 v[42:45], v[160:163], v[220:223], v[42:45]
	v_mfma_f32_16x16x32_f16 v[46:49], v[160:163], v[224:227], v[46:49]
	v_mfma_f32_16x16x32_f16 v[34:37], v[160:163], v[228:231], v[34:37]
	v_add_u32_e32 v98, s73, v98
	ds_read_b128 v[160:163], v98
	ds_read_b128 v[220:223], v98 offset:16384
	ds_read_b128 v[224:227], v98 offset:32768
	ds_read_b128 v[228:231], v98 offset:49152
	s_add_i32 s8, s22, s42
	s_waitcnt vmcnt(15) lgkmcnt(7)
	v_mfma_f32_16x16x32_f16 v[164:167], v[66:69], v[188:191], v[164:167]
	s_waitcnt lgkmcnt(6)
	v_mfma_f32_16x16x32_f16 v[168:171], v[66:69], v[208:211], v[168:171]
	s_waitcnt lgkmcnt(5)
	v_mfma_f32_16x16x32_f16 v[172:175], v[66:69], v[212:215], v[172:175]
	s_waitcnt lgkmcnt(4)
	v_mfma_f32_16x16x32_f16 v[66:69], v[66:69], v[216:219], v[78:81]
	s_waitcnt vmcnt(14)
	v_mfma_f32_16x16x32_f16 v[58:61], v[192:195], v[188:191], v[58:61]
	v_mfma_f32_16x16x32_f16 v[78:81], v[192:195], v[208:211], v[82:85]
	v_mfma_f32_16x16x32_f16 v[82:85], v[192:195], v[212:215], v[86:89]
	v_mfma_f32_16x16x32_f16 v[70:73], v[192:195], v[216:219], v[70:73]
	s_waitcnt vmcnt(13)
	v_mfma_f32_16x16x32_f16 v[54:57], v[196:199], v[188:191], v[54:57]
	v_mfma_f32_16x16x32_f16 v[74:77], v[196:199], v[208:211], v[74:77]
	v_mfma_f32_16x16x32_f16 v[86:89], v[196:199], v[212:215], v[90:93]
	v_mfma_f32_16x16x32_f16 v[62:65], v[196:199], v[216:219], v[62:65]
	s_waitcnt vmcnt(12)
	v_mfma_f32_16x16x32_f16 v[38:41], v[200:203], v[188:191], v[38:41]
	buffer_load_dwordx4 v[90:93], v147, s[16:19], s8 offen
	buffer_load_dwordx4 v[188:191], v148, s[16:19], s8 offen
	buffer_load_dwordx4 v[192:195], v149, s[16:19], s8 offen
	buffer_load_dwordx4 v[196:199], v150, s[16:19], s8 offen
	v_mfma_f32_16x16x32_f16 v[42:45], v[200:203], v[208:211], v[42:45]
	v_mfma_f32_16x16x32_f16 v[46:49], v[200:203], v[212:215], v[46:49]
	v_mfma_f32_16x16x32_f16 v[34:37], v[200:203], v[216:219], v[34:37]
	v_add_u32_e32 v99, s74, v99
	ds_read_b128 v[200:203], v99
	ds_read_b128 v[208:211], v99 offset:16384
	ds_read_b128 v[212:215], v99 offset:32768
	ds_read_b128 v[216:219], v99 offset:49152
	s_add_i32 s8, s22, s43
	s_waitcnt vmcnt(15) lgkmcnt(7)
	v_mfma_f32_16x16x32_f16 v[164:167], v[50:53], v[160:163], v[164:167]
	s_waitcnt lgkmcnt(6)
	v_mfma_f32_16x16x32_f16 v[168:171], v[50:53], v[220:223], v[168:171]
	s_waitcnt lgkmcnt(5)
	v_mfma_f32_16x16x32_f16 v[172:175], v[50:53], v[224:227], v[172:175]
	s_waitcnt lgkmcnt(4)
	v_mfma_f32_16x16x32_f16 v[50:53], v[50:53], v[228:231], v[66:69]
	s_waitcnt vmcnt(14)
	v_mfma_f32_16x16x32_f16 v[58:61], v[140:143], v[160:163], v[58:61]
	v_mfma_f32_16x16x32_f16 v[66:69], v[140:143], v[220:223], v[78:81]
	v_mfma_f32_16x16x32_f16 v[78:81], v[140:143], v[224:227], v[82:85]
	v_mfma_f32_16x16x32_f16 v[70:73], v[140:143], v[228:231], v[70:73]
	s_waitcnt vmcnt(13)
	v_mfma_f32_16x16x32_f16 v[54:57], v[152:155], v[160:163], v[54:57]
	v_mfma_f32_16x16x32_f16 v[74:77], v[152:155], v[220:223], v[74:77]
	v_mfma_f32_16x16x32_f16 v[82:85], v[152:155], v[224:227], v[86:89]
	v_mfma_f32_16x16x32_f16 v[62:65], v[152:155], v[228:231], v[62:65]
	s_waitcnt vmcnt(12)
	v_mfma_f32_16x16x32_f16 v[38:41], v[176:179], v[160:163], v[38:41]
	buffer_load_dwordx4 v[86:89], v147, s[16:19], s8 offen
	buffer_load_dwordx4 v[140:143], v148, s[16:19], s8 offen
	buffer_load_dwordx4 v[152:155], v149, s[16:19], s8 offen
	buffer_load_dwordx4 v[160:163], v150, s[16:19], s8 offen
	v_mfma_f32_16x16x32_f16 v[42:45], v[176:179], v[220:223], v[42:45]
	v_mfma_f32_16x16x32_f16 v[46:49], v[176:179], v[224:227], v[46:49]
	v_mfma_f32_16x16x32_f16 v[34:37], v[176:179], v[228:231], v[34:37]
	v_add_u32_e32 v100, s75, v100
	ds_read_b128 v[176:179], v100
	ds_read_b128 v[220:223], v100 offset:16384
	ds_read_b128 v[224:227], v100 offset:32768
	ds_read_b128 v[228:231], v100 offset:49152
	s_add_i32 s8, s22, s44
	s_waitcnt vmcnt(15) lgkmcnt(7)
	v_mfma_f32_16x16x32_f16 v[164:167], v[126:129], v[200:203], v[164:167]
	s_waitcnt lgkmcnt(6)
	v_mfma_f32_16x16x32_f16 v[168:171], v[126:129], v[208:211], v[168:171]
	s_waitcnt lgkmcnt(5)
	v_mfma_f32_16x16x32_f16 v[172:175], v[126:129], v[212:215], v[172:175]
	s_waitcnt lgkmcnt(4)
	v_mfma_f32_16x16x32_f16 v[50:53], v[126:129], v[216:219], v[50:53]
	s_waitcnt vmcnt(14)
	v_mfma_f32_16x16x32_f16 v[58:61], v[136:139], v[200:203], v[58:61]
	v_mfma_f32_16x16x32_f16 v[66:69], v[136:139], v[208:211], v[66:69]
	v_mfma_f32_16x16x32_f16 v[78:81], v[136:139], v[212:215], v[78:81]
	v_mfma_f32_16x16x32_f16 v[70:73], v[136:139], v[216:219], v[70:73]
	s_waitcnt vmcnt(13)
	v_mfma_f32_16x16x32_f16 v[54:57], v[184:187], v[200:203], v[54:57]
	v_mfma_f32_16x16x32_f16 v[74:77], v[184:187], v[208:211], v[74:77]
	v_mfma_f32_16x16x32_f16 v[82:85], v[184:187], v[212:215], v[82:85]
	v_mfma_f32_16x16x32_f16 v[62:65], v[184:187], v[216:219], v[62:65]
	s_waitcnt vmcnt(12)
	v_mfma_f32_16x16x32_f16 v[38:41], v[204:207], v[200:203], v[38:41]
	buffer_load_dwordx4 v[126:129], v147, s[16:19], s8 offen
	buffer_load_dwordx4 v[136:139], v148, s[16:19], s8 offen
	buffer_load_dwordx4 v[184:187], v149, s[16:19], s8 offen
	buffer_load_dwordx4 v[200:203], v150, s[16:19], s8 offen
	v_mfma_f32_16x16x32_f16 v[42:45], v[204:207], v[208:211], v[42:45]
	v_mfma_f32_16x16x32_f16 v[46:49], v[204:207], v[212:215], v[46:49]
	v_mfma_f32_16x16x32_f16 v[34:37], v[204:207], v[216:219], v[34:37]
	v_add_u32_e32 v111, s76, v111
	ds_read_b128 v[204:207], v111
	ds_read_b128 v[208:211], v111 offset:16384
	ds_read_b128 v[212:215], v111 offset:32768
	ds_read_b128 v[216:219], v111 offset:49152
	s_add_i32 s8, s22, s45
	s_waitcnt vmcnt(15) lgkmcnt(7)
	v_mfma_f32_16x16x32_f16 v[164:167], v[94:97], v[176:179], v[164:167]
	s_waitcnt lgkmcnt(6)
	v_mfma_f32_16x16x32_f16 v[168:171], v[94:97], v[220:223], v[168:171]
	s_waitcnt vmcnt(14)
	v_mfma_f32_16x16x32_f16 v[58:61], v[122:125], v[176:179], v[58:61]
	v_mfma_f32_16x16x32_f16 v[66:69], v[122:125], v[220:223], v[66:69]
	s_waitcnt lgkmcnt(5)
	v_mfma_f32_16x16x32_f16 v[78:81], v[122:125], v[224:227], v[78:81]
	s_waitcnt lgkmcnt(4)
	v_mfma_f32_16x16x32_f16 v[70:73], v[122:125], v[228:231], v[70:73]
	s_waitcnt vmcnt(13)
	v_mfma_f32_16x16x32_f16 v[54:57], v[156:159], v[176:179], v[54:57]
	v_mfma_f32_16x16x32_f16 v[74:77], v[156:159], v[220:223], v[74:77]
	v_mfma_f32_16x16x32_f16 v[82:85], v[156:159], v[224:227], v[82:85]
	v_mfma_f32_16x16x32_f16 v[62:65], v[156:159], v[228:231], v[62:65]
	s_waitcnt vmcnt(12)
	v_mfma_f32_16x16x32_f16 v[38:41], v[180:183], v[176:179], v[38:41]
	v_mfma_f32_16x16x32_f16 v[42:45], v[180:183], v[220:223], v[42:45]
	buffer_load_dwordx4 v[122:125], v147, s[16:19], s8 offen
	buffer_load_dwordx4 v[156:159], v148, s[16:19], s8 offen
	buffer_load_dwordx4 v[176:179], v149, s[16:19], s8 offen
	buffer_load_dwordx4 v[220:223], v150, s[16:19], s8 offen
	v_mfma_f32_16x16x32_f16 v[50:53], v[94:97], v[228:231], v[50:53]
	v_mfma_f32_16x16x32_f16 v[46:49], v[180:183], v[224:227], v[46:49]
	v_mfma_f32_16x16x32_f16 v[34:37], v[180:183], v[228:231], v[34:37]
	v_mfma_f32_16x16x32_f16 v[172:175], v[94:97], v[224:227], v[172:175]
	v_add_u32_e32 v98, s77, v98
	ds_read_b128 v[94:97], v98
	ds_read_b128 v[180:183], v98 offset:16384
	ds_read_b128 v[224:227], v98 offset:32768
	ds_read_b128 v[228:231], v98 offset:49152
	s_add_i32 s8, s22, s46
	s_waitcnt vmcnt(15) lgkmcnt(7)
	v_mfma_f32_16x16x32_f16 v[164:167], v[90:93], v[204:207], v[164:167]
	s_waitcnt lgkmcnt(6)
	v_mfma_f32_16x16x32_f16 v[168:171], v[90:93], v[208:211], v[168:171]
	s_waitcnt lgkmcnt(5)
	v_mfma_f32_16x16x32_f16 v[172:175], v[90:93], v[212:215], v[172:175]
	s_waitcnt lgkmcnt(4)
	v_mfma_f32_16x16x32_f16 v[90:93], v[90:93], v[216:219], v[50:53]
	s_waitcnt vmcnt(14)
	v_mfma_f32_16x16x32_f16 v[232:235], v[188:191], v[204:207], v[58:61]
	v_mfma_f32_16x16x32_f16 v[66:69], v[188:191], v[208:211], v[66:69]
	v_mfma_f32_16x16x32_f16 v[78:81], v[188:191], v[212:215], v[78:81]
	v_mfma_f32_16x16x32_f16 v[70:73], v[188:191], v[216:219], v[70:73]
	s_waitcnt vmcnt(13)
	v_mfma_f32_16x16x32_f16 v[188:191], v[192:195], v[204:207], v[54:57]
	v_mfma_f32_16x16x32_f16 v[74:77], v[192:195], v[208:211], v[74:77]
	v_mfma_f32_16x16x32_f16 v[82:85], v[192:195], v[212:215], v[82:85]
	v_mfma_f32_16x16x32_f16 v[62:65], v[192:195], v[216:219], v[62:65]
	s_waitcnt vmcnt(12)
	v_mfma_f32_16x16x32_f16 v[192:195], v[196:199], v[204:207], v[38:41]
	buffer_load_dwordx4 v[58:61], v147, s[16:19], s8 offen
	buffer_load_dwordx4 v[54:57], v148, s[16:19], s8 offen
	buffer_load_dwordx4 v[50:53], v149, s[16:19], s8 offen
	buffer_load_dwordx4 v[38:41], v150, s[16:19], s8 offen
	v_mfma_f32_16x16x32_f16 v[42:45], v[196:199], v[208:211], v[42:45]
	v_mfma_f32_16x16x32_f16 v[46:49], v[196:199], v[212:215], v[46:49]
	v_mfma_f32_16x16x32_f16 v[196:199], v[196:199], v[216:219], v[34:37]
	v_add_u32_e32 v99, s78, v99
	ds_read_b128 v[204:207], v99
	ds_read_b128 v[208:211], v99 offset:16384
	ds_read_b128 v[212:215], v99 offset:32768
	ds_read_b128 v[216:219], v99 offset:49152
	s_add_i32 s8, s22, s47
	s_waitcnt vmcnt(15) lgkmcnt(7)
	v_mfma_f32_16x16x32_f16 v[164:167], v[86:89], v[94:97], v[164:167]
	s_waitcnt lgkmcnt(6)
	v_mfma_f32_16x16x32_f16 v[168:171], v[86:89], v[180:183], v[168:171]
	s_waitcnt lgkmcnt(5)
	v_mfma_f32_16x16x32_f16 v[172:175], v[86:89], v[224:227], v[172:175]
	s_waitcnt lgkmcnt(4)
	v_mfma_f32_16x16x32_f16 v[86:89], v[86:89], v[228:231], v[90:93]
	s_waitcnt vmcnt(14)
	v_mfma_f32_16x16x32_f16 v[232:235], v[140:143], v[94:97], v[232:235]
	v_mfma_f32_16x16x32_f16 v[66:69], v[140:143], v[180:183], v[66:69]
	v_mfma_f32_16x16x32_f16 v[236:239], v[140:143], v[224:227], v[78:81]
	v_mfma_f32_16x16x32_f16 v[70:73], v[140:143], v[228:231], v[70:73]
	s_waitcnt vmcnt(13)
	v_mfma_f32_16x16x32_f16 v[140:143], v[152:155], v[94:97], v[188:191]
	v_mfma_f32_16x16x32_f16 v[74:77], v[152:155], v[180:183], v[74:77]
	v_mfma_f32_16x16x32_f16 v[82:85], v[152:155], v[224:227], v[82:85]
	v_mfma_f32_16x16x32_f16 v[62:65], v[152:155], v[228:231], v[62:65]
	s_waitcnt vmcnt(12)
	v_mfma_f32_16x16x32_f16 v[152:155], v[160:163], v[94:97], v[192:195]
	buffer_load_dwordx4 v[94:97], v147, s[16:19], s8 offen
	buffer_load_dwordx4 v[90:93], v148, s[16:19], s8 offen
	buffer_load_dwordx4 v[78:81], v149, s[16:19], s8 offen
	buffer_load_dwordx4 v[34:37], v150, s[16:19], s8 offen
	v_mfma_f32_16x16x32_f16 v[42:45], v[160:163], v[180:183], v[42:45]
	v_mfma_f32_16x16x32_f16 v[46:49], v[160:163], v[224:227], v[46:49]
	v_mfma_f32_16x16x32_f16 v[160:163], v[160:163], v[228:231], v[196:199]
	v_add_u32_e32 v100, s79, v100
	ds_read_b128 v[180:183], v100
	ds_read_b128 v[188:191], v100 offset:16384
	ds_read_b128 v[192:195], v100 offset:32768
	ds_read_b128 v[196:199], v100 offset:49152
	s_add_i32 s8, s22, s48
	s_waitcnt vmcnt(15) lgkmcnt(7)
	v_mfma_f32_16x16x32_f16 v[164:167], v[126:129], v[204:207], v[164:167]
	s_waitcnt lgkmcnt(6)
	v_mfma_f32_16x16x32_f16 v[168:171], v[126:129], v[208:211], v[168:171]
	s_waitcnt lgkmcnt(5)
	v_mfma_f32_16x16x32_f16 v[172:175], v[126:129], v[212:215], v[172:175]
	s_waitcnt lgkmcnt(4)
	v_mfma_f32_16x16x32_f16 v[86:89], v[126:129], v[216:219], v[86:89]
	s_waitcnt vmcnt(14)
	v_mfma_f32_16x16x32_f16 v[126:129], v[136:139], v[204:207], v[232:235]
	v_mfma_f32_16x16x32_f16 v[66:69], v[136:139], v[208:211], v[66:69]
	v_mfma_f32_16x16x32_f16 v[224:227], v[136:139], v[212:215], v[236:239]
	v_mfma_f32_16x16x32_f16 v[136:139], v[136:139], v[216:219], v[70:73]
	s_waitcnt vmcnt(13)
	v_mfma_f32_16x16x32_f16 v[140:143], v[184:187], v[204:207], v[140:143]
	v_mfma_f32_16x16x32_f16 v[74:77], v[184:187], v[208:211], v[74:77]
	v_mfma_f32_16x16x32_f16 v[228:231], v[184:187], v[212:215], v[82:85]
	v_mfma_f32_16x16x32_f16 v[184:187], v[184:187], v[216:219], v[62:65]
	s_waitcnt vmcnt(12)
	v_mfma_f32_16x16x32_f16 v[152:155], v[200:203], v[204:207], v[152:155]
	v_mfma_f32_16x16x32_f16 v[204:207], v[200:203], v[208:211], v[42:45]
	buffer_load_dwordx4 v[82:85], v147, s[16:19], s8 offen
	buffer_load_dwordx4 v[70:73], v148, s[16:19], s8 offen
	buffer_load_dwordx4 v[62:65], v149, s[16:19], s8 offen
	buffer_load_dwordx4 v[42:45], v150, s[16:19], s8 offen
	v_mfma_f32_16x16x32_f16 v[46:49], v[200:203], v[212:215], v[46:49]
	v_mfma_f32_16x16x32_f16 v[160:163], v[200:203], v[216:219], v[160:163]
	v_add_u32_e32 v0, 0x1ac00, v104
	ds_read_b128 v[240:243], v0
	ds_read_b128 v[244:247], v0 offset:16
	s_waitcnt vmcnt(12) lgkmcnt(5)
	v_mfma_f32_16x16x32_f16 v[164:167], v[122:125], v[180:183], v[164:167]
	v_mfma_f32_16x16x32_f16 v[126:129], v[156:159], v[180:183], v[126:129]
	v_mfma_f32_16x16x32_f16 v[140:143], v[176:179], v[180:183], v[140:143]
	v_mfma_f32_16x16x32_f16 v[152:155], v[220:223], v[180:183], v[152:155]
	s_waitcnt lgkmcnt(4)
	v_mfma_f32_16x16x32_f16 v[168:171], v[122:125], v[188:191], v[168:171]
	v_mfma_f32_16x16x32_f16 v[208:211], v[156:159], v[188:191], v[66:69]
	v_mfma_f32_16x16x32_f16 v[212:215], v[176:179], v[188:191], v[74:77]
	v_mfma_f32_16x16x32_f16 v[204:207], v[220:223], v[188:191], v[204:207]
	s_waitcnt lgkmcnt(3)
	v_mfma_f32_16x16x32_f16 v[172:175], v[122:125], v[192:195], v[172:175]
	v_cvt_pk_f16_f32 v232, v164, v165
	v_cvt_pk_f16_f32 v233, v166, v167
	v_pk_max_f16 v232, v232, 0
	v_pk_max_f16 v233, v233, 0
	v_mfma_f32_16x16x32_f16 v[224:227], v[156:159], v[192:195], v[224:227]
	v_cvt_pk_f16_f32 v234, v126, v127
	v_cvt_pk_f16_f32 v235, v128, v129
	v_pk_max_f16 v234, v234, 0
	v_pk_max_f16 v235, v235, 0
	v_mfma_f32_16x16x32_f16 v[228:231], v[176:179], v[192:195], v[228:231]
	v_cvt_pk_f16_f32 v236, v140, v141
	v_cvt_pk_f16_f32 v237, v142, v143
	v_pk_max_f16 v236, v236, 0
	v_pk_max_f16 v237, v237, 0
	v_mfma_f32_16x16x32_f16 v[216:219], v[220:223], v[192:195], v[46:49]
	v_cvt_pk_f16_f32 v238, v152, v153
	v_cvt_pk_f16_f32 v239, v154, v155
	v_pk_max_f16 v238, v238, 0
	v_pk_max_f16 v239, v239, 0
	s_waitcnt lgkmcnt(2)
	v_mfma_f32_16x16x32_f16 v[200:203], v[122:125], v[196:199], v[86:89]
	v_cvt_pk_f16_f32 v180, v168, v169
	v_cvt_pk_f16_f32 v181, v170, v171
	v_pk_max_f16 v180, v180, 0
	v_pk_max_f16 v181, v181, 0
	s_add_i32 s8, s22, s49
	buffer_load_dwordx4 v[86:89], v147, s[16:19], s8 offen
	buffer_load_dwordx4 v[74:77], v148, s[16:19], s8 offen
	buffer_load_dwordx4 v[66:69], v149, s[16:19], s8 offen
	buffer_load_dwordx4 v[46:49], v150, s[16:19], s8 offen
	v_mfma_f32_16x16x32_f16 v[136:139], v[156:159], v[196:199], v[136:139]
	v_cvt_pk_f16_f32 v182, v208, v209
	v_cvt_pk_f16_f32 v183, v210, v211
	v_pk_max_f16 v182, v182, 0
	v_pk_max_f16 v183, v183, 0
	s_waitcnt lgkmcnt(1)
	v_mfma_f32_16x16x32_f16 v[252:255], v[240:243], v[232:235], 0
	v_cvt_pk_f16_f32 v232, v172, v173
	v_cvt_pk_f16_f32 v233, v174, v175
	v_pk_max_f16 v232, v232, 0
	v_pk_max_f16 v233, v233, 0
	v_mfma_f32_16x16x32_f16 v[184:187], v[176:179], v[196:199], v[184:187]
	v_cvt_pk_f16_f32 v188, v212, v213
	v_cvt_pk_f16_f32 v189, v214, v215
	v_pk_max_f16 v188, v188, 0
	v_pk_max_f16 v189, v189, 0
	s_waitcnt lgkmcnt(0)
	v_mfma_f32_16x16x32_f16 v[252:255], v[244:247], v[236:239], v[252:255]
	ds_read_u16 v102, v114
	ds_read_u16 v103, v114 offset:512
	ds_read_u16 v115, v114 offset:1024
	ds_read_u16 v116, v114 offset:1536
	v_cvt_pk_f16_f32 v234, v224, v225
	v_cvt_pk_f16_f32 v235, v226, v227
	v_pk_max_f16 v234, v234, 0
	v_pk_max_f16 v235, v235, 0
	v_mfma_f32_16x16x32_f16 v[160:163], v[220:223], v[196:199], v[160:163]
	v_cvt_pk_f16_f32 v190, v204, v205
	v_cvt_pk_f16_f32 v191, v206, v207
	v_pk_max_f16 v190, v190, 0
	v_pk_max_f16 v191, v191, 0
	v_mfma_f32_16x16x32_f16 v[192:195], v[240:243], v[180:183], 0
	v_cvt_pk_f16_f32 v236, v228, v229
	v_cvt_pk_f16_f32 v237, v230, v231
	v_pk_max_f16 v236, v236, 0
	v_pk_max_f16 v237, v237, 0
	v_mfma_f32_16x16x32_f16 v[192:195], v[244:247], v[188:191], v[192:195]
	v_cvt_pk_f16_f32 v238, v216, v217
	v_cvt_pk_f16_f32 v239, v218, v219
	v_pk_max_f16 v238, v238, 0
	v_pk_max_f16 v239, v239, 0
	v_cvt_pk_f16_f32 v180, v200, v201
	v_cvt_pk_f16_f32 v181, v202, v203
	v_pk_max_f16 v180, v180, 0
	v_pk_max_f16 v181, v181, 0
	v_mfma_f32_16x16x32_f16 v[196:199], v[240:243], v[232:235], 0
	v_cvt_pk_f16_f32 v182, v136, v137
	v_cvt_pk_f16_f32 v183, v138, v139
	v_pk_max_f16 v182, v182, 0
	v_pk_max_f16 v183, v183, 0
	v_mfma_f32_16x16x32_f16 v[196:199], v[244:247], v[236:239], v[196:199]
	v_cvt_pk_f16_f32 v188, v184, v185
	v_cvt_pk_f16_f32 v189, v186, v187
	v_pk_max_f16 v188, v188, 0
	v_pk_max_f16 v189, v189, 0
	v_cvt_pk_f16_f32 v190, v160, v161
	v_cvt_pk_f16_f32 v191, v162, v163
	v_pk_max_f16 v190, v190, 0
	v_pk_max_f16 v191, v191, 0
	v_mfma_f32_16x16x32_f16 v[122:125], v[240:243], v[180:183], 0
	s_nop 0
	v_mfma_f32_16x16x32_f16 v[122:125], v[244:247], v[188:191], v[122:125]
	v_add_u32_e32 v145, 0x12c00, v105
	ds_read_b128 v[240:243], v145 offset:2048
	ds_read_b128 v[244:247], v145 offset:2064
	ds_read_b128 v[248:251], v145 offset:2080
	s_load_dword s30, s[12:13], 0x0
	v_cndmask_b32_e64 v0, v252, v192, s[2:3]
	ds_read_b128 v[252:255], v145 offset:2096
	v_cndmask_b32_e64 v0, v0, v196, s[0:1]
	v_cndmask_b32_e64 v0, v0, v122, s[26:27]
	ds_write_b32 v112, v0
	s_waitcnt vmcnt(16)
	v_cndmask_b32_e64 v1, v30, v134, s[0:1]
	v_bfi_b32 v30, s10, v1, v30
	v_perm_b32 v1, v22, v134, s24
	v_cndmask_b32_e64 v22, v22, v1, s[0:1]
	v_bfi_b32 v1, s10, v135, v18
	v_perm_b32 v121, v10, v135, s24
	v_cndmask_b32_e64 v18, v18, v1, s[0:1]
	v_cndmask_b32_e64 v10, v10, v121, s[0:1]
	s_add_i32 s22, s22, 0x80000
	s_add_i32 s11, s11, 1
	s_add_u32 s12, s12, 4
	s_addc_u32 s13, s13, 0
	v_add_u32_e32 v104, 0x400, v104
	v_add_u32_e32 v105, 0x800, v105
	v_add_u32_e32 v114, 2, v114
	s_cmp_eq_u32 s22, 0x898000
	s_waitcnt lgkmcnt(0)
	s_barrier
	ds_read_b128 v[232:235], v113
	ds_read_b128 v[236:239], v113 offset:1024
	s_waitcnt lgkmcnt(0)
	v_add_f32_e32 v0, v232, v233
	v_add_f32_e32 v1, v234, v235
	v_add_f32_e32 v121, v236, v237
	v_add_f32_e32 v144, v238, v239
	v_add_f32_e32 v0, v0, v1
	v_add_f32_e32 v121, v121, v144
	v_add_f32_e32 v0, v0, v121
	v_add_f32_e32 v0, s30, v0
	v_cvt_f16_f32_e32 v1, v0
	v_cvt_f16_f32_e32 v121, v0
	ds_write_b32 v106, v0
	v_add_u32_e32 v106, 4, v106
	v_permlane16_swap_b32_e32 v1, v121
	s_cbranch_scc0 .LBB1_4
